# speedup vs baseline: 1.0124x; 1.0124x over previous
.LBB0_17:
	v_mfma_f32_32x32x16_bf16 v[112:127], a[192:195], a[128:131], v[0:15]
	v_exp_f32_e32 v48, v48
	v_exp_f32_e32 v49, v49
	ds_read_b64_tr_b16 v[172:173], v215 offset:0
	v_mfma_f32_32x32x16_bf16 v[96:111], a[192:195], a[160:163], v[16:31]
	v_cvt_pk_bf16_f32 v164, v128, v129
	v_exp_f32_e32 v50, v50
	v_exp_f32_e32 v51, v51
	v_mfma_f32_32x32x16_bf16 v[80:95], a[224:227], a[128:131], v[0:15]
	ds_read_b64_tr_b16 v[174:175], v215 offset:0x800
	v_cvt_pk_bf16_f32 v165, v130, v131
	ds_read_b64_tr_b16 v[184:185], v215 offset:0x200
	v_exp_f32_e32 v239, v52
	v_mfma_f32_32x32x16_bf16 v[64:79], a[224:227], a[160:163], v[16:31]
	v_exp_f32_e32 v240, v53
	v_cvt_pk_bf16_f32 v166, v132, v133
	ds_read_b64_tr_b16 v[186:187], v215 offset:0xa00
	ds_read_b64_tr_b16 v[180:181], v215 offset:0x400
	v_mfma_f32_32x32x16_bf16 v[112:127], a[196:199], a[132:135], v[112:127]
	v_exp_f32_e32 v241, v54
	v_exp_f32_e32 v242, v55
	v_cvt_pk_bf16_f32 v167, v134, v135
	v_mfma_f32_32x32x16_bf16 v[96:111], a[196:199], a[164:167], v[96:111]
	v_exp_f32_e32 v227, v56
	v_exp_f32_e32 v228, v57
	ds_read_b64_tr_b16 v[182:183], v215 offset:0xc00
	v_mfma_f32_32x32x16_bf16 v[80:95], a[228:231], a[132:135], v[80:95]
	v_cvt_pk_bf16_f32 v128, v136, v137
	v_exp_f32_e32 v229, v58
	v_exp_f32_e32 v230, v59
	v_mfma_f32_32x32x16_bf16 v[64:79], a[228:231], a[164:167], v[64:79]
	ds_read_b64_tr_b16 v[188:189], v215 offset:0x600
	v_cvt_pk_bf16_f32 v129, v138, v139
	v_exp_f32_e32 v231, v60
	v_exp_f32_e32 v232, v61
	v_mfma_f32_32x32x16_bf16 v[112:127], a[200:203], a[136:139], v[112:127]
	ds_read_b64_tr_b16 v[190:191], v215 offset:0xe00
	v_cvt_pk_bf16_f32 v130, v140, v141
	ds_read_b64_tr_b16 v[176:177], v215 offset:0x1000
	v_exp_f32_e32 v233, v62
	v_mfma_f32_32x32x16_bf16 v[96:111], a[200:203], a[168:171], v[96:111]
	v_exp_f32_e32 v234, v63
	ds_read_b64_tr_b16 v[178:179], v215 offset:0x1800
	v_cvt_pk_bf16_f32 v131, v142, v143
	v_exp_f32_e32 v141, v32
	v_mfma_f32_32x32x16_bf16 v[80:95], a[232:235], a[136:139], v[80:95]
	v_exp_f32_e32 v142, v33
	ds_read_b64_tr_b16 v[168:169], v215 offset:0x1200
	v_cvt_pk_bf16_f32 v192, v144, v145
	v_exp_f32_e32 v143, v34
	v_mfma_f32_32x32x16_bf16 v[64:79], a[232:235], a[168:171], v[64:79]
	ds_read_b64_tr_b16 v[170:171], v215 offset:0x1a00
	v_exp_f32_e32 v243, v35
	v_cvt_pk_bf16_f32 v193, v146, v147
	ds_read_b64_tr_b16 v[160:161], v215 offset:0x1400
	v_mfma_f32_32x32x16_bf16 v[112:127], a[204:207], a[140:143], v[112:127]
	v_exp_f32_e32 v244, v36
	v_exp_f32_e32 v245, v37
	v_cvt_pk_bf16_f32 v194, v148, v149
	v_mfma_f32_32x32x16_bf16 v[96:111], a[204:207], a[172:175], v[96:111]
	ds_read_b64_tr_b16 v[162:163], v215 offset:0x1c00
	ds_read_b64_tr_b16 v[136:137], v215 offset:0x1600
	v_exp_f32_e32 v246, v38
	v_exp_f32_e32 v247, v39
	v_mfma_f32_32x32x16_bf16 v[80:95], a[236:239], a[140:143], v[80:95]
	v_cvt_pk_bf16_f32 v195, v150, v151
	v_exp_f32_e32 v148, v40
	v_exp_f32_e32 v149, v41
	v_mfma_f32_32x32x16_bf16 v[64:79], a[236:239], a[172:175], v[64:79]
	ds_read_b64_tr_b16 v[138:139], v215 offset:0x1e00
	v_cvt_pk_bf16_f32 v144, v152, v153
	v_exp_f32_e32 v150, v42
	v_exp_f32_e32 v151, v43
	v_mfma_f32_32x32x16_bf16 v[112:127], a[208:211], a[144:147], v[112:127]
	ds_read_b64_tr_b16 v[132:133], v215 offset:0x2000
	v_cvt_pk_bf16_f32 v145, v154, v155
	v_exp_f32_e32 v152, v44
	v_exp_f32_e32 v153, v45
	v_mfma_f32_32x32x16_bf16 v[96:111], a[208:211], a[176:179], v[96:111]
	ds_read_b64_tr_b16 v[134:135], v215 offset:0x2800
	v_cvt_pk_bf16_f32 v146, v156, v157
	ds_read_b64_tr_b16 v[60:61], v215 offset:0x2200
	v_exp_f32_e32 v154, v46
	v_mfma_f32_32x32x16_bf16 v[80:95], a[240:243], a[144:147], v[80:95]
	v_exp_f32_e32 v155, v47
	ds_read_b64_tr_b16 v[62:63], v215 offset:0x2a00
	v_cvt_pk_bf16_f32 v147, v158, v159
	s_mov_b32 s0, s29
	ds_read_b64_tr_b16 v[56:57], v215 offset:0x2400
	v_mfma_f32_32x32x16_bf16 v[64:79], a[240:243], a[176:179], v[64:79]
	v_cvt_pk_bf16_f32 v52, v48, v49
	v_add_f32_e32 v32, v236, v48
	v_add_f32_e32 v33, v235, v49
	s_add_i32 s57, s58, s59
	s_and_b32 s57, s57, 0x7ffff
	s_mov_b32 s33, s57
	s_mov_b32 s1, s33
	v_mfma_f32_32x32x16_bf16 v[112:127], a[212:215], a[148:151], v[112:127]
	ds_read_b64_tr_b16 v[58:59], v215 offset:0x2c00
	v_cvt_pk_bf16_f32 v53, v50, v51
	v_add_f32_e32 v32, v32, v50
	v_add_f32_e32 v33, v33, v51
	s_mov_b32 s35, s20
	ds_read_b64_tr_b16 v[48:49], v215 offset:0x2600
	v_mfma_f32_32x32x16_bf16 v[96:111], a[212:215], a[180:183], v[96:111]
	v_cvt_pk_bf16_f32 v54, v239, v240
	v_add_f32_e32 v32, v32, v239
	v_add_f32_e32 v33, v33, v240
	s_add_i32 s36, s57, 0x400
	ds_read_b64_tr_b16 v[50:51], v215 offset:0x2e00
	ds_read_b64_tr_b16 v[44:45], v215 offset:0x3000
	v_mfma_f32_32x32x16_bf16 v[80:95], a[244:247], a[148:151], v[80:95]
	v_cvt_pk_bf16_f32 v55, v241, v242
	v_add_f32_e32 v32, v32, v241
	v_add_f32_e32 v33, v33, v242
	s_mov_b32 s37, s21
	ds_read_b64_tr_b16 v[46:47], v215 offset:0x3800
	v_add_f32_e32 v32, v32, v227
	v_mfma_f32_32x32x16_bf16 v[64:79], a[244:247], a[180:183], v[64:79]
	v_add_f32_e32 v33, v33, v228
	s_add_i32 s34, s57, 0x800
	s_mov_b32 s38, s34
	ds_read_b64_tr_b16 v[40:41], v215 offset:0x3200
	v_add_f32_e32 v32, v32, v229
	v_add_f32_e32 v33, v33, v230
	v_mfma_f32_32x32x16_bf16 v[112:127], a[216:219], a[152:155], v[112:127]
	s_mov_b32 s39, s22
	ds_read_b64_tr_b16 v[42:43], v215 offset:0x3a00
	v_add_f32_e32 v32, v32, v231
	v_add_f32_e32 v33, v33, v232
	s_add_i32 s40, s57, 0xc00
	ds_read_b64_tr_b16 v[36:37], v215 offset:0x3400
	v_mfma_f32_32x32x16_bf16 v[96:111], a[216:219], a[184:187], v[96:111]
	ds_read_b64_tr_b16 v[38:39], v215 offset:0x3c00
	v_add_f32_e32 v156, v32, v233
	v_add_f32_e32 v157, v33, v234
	s_mov_b32 s41, s23
	ds_read_b64_tr_b16 v[32:33], v215 offset:0x3600
	v_cvt_pk_bf16_f32 v140, v141, v142
	v_mfma_f32_32x32x16_bf16 v[80:95], a[248:251], a[152:155], v[80:95]
	v_add_f32_e32 v158, v237, v141
	v_add_f32_e32 v142, v238, v142
	s_mov_b32 s42, s58
	ds_read_b64_tr_b16 v[34:35], v215 offset:0x3e00
	v_cvt_pk_bf16_f32 v141, v143, v243
	v_add_f32_e32 v143, v158, v143
	v_mfma_f32_32x32x16_bf16 v[64:79], a[248:251], a[184:187], v[64:79]
	v_add_f32_e32 v158, v142, v243
	s_mov_b32 s43, s24
	v_cvt_pk_bf16_f32 v142, v244, v245
	v_add_f32_e32 v159, v143, v244
	v_add_f32_e32 v158, v158, v245
	s_add_i32 s44, s58, 0x80
	v_mfma_f32_32x32x16_bf16 v[112:127], a[220:223], a[156:159], v[112:127]
	v_cvt_pk_bf16_f32 v143, v246, v247
	v_add_f32_e32 v159, v159, v246
	v_add_f32_e32 v158, v158, v247
	s_mov_b32 s45, s25
	v_add_f32_e32 v159, v159, v148
	v_add_f32_e32 v158, v158, v149
	v_mfma_f32_32x32x16_bf16 v[96:111], a[220:223], a[188:191], v[96:111]
	s_add_i32 s46, s58, 0x800
	v_add_f32_e32 v159, v159, v150
	v_add_f32_e32 v158, v158, v151
	s_mov_b32 s47, s26
	v_add_f32_e32 v159, v159, v152
	v_add_f32_e32 v158, v158, v153
	v_mfma_f32_32x32x16_bf16 v[80:95], a[252:255], a[156:159], v[80:95]
	s_add_i32 s48, s58, 0x880
	v_add_f32_e32 v159, v159, v154
	v_add_f32_e32 v158, v158, v155
	v_add_f32_e32 v156, v156, v157
	v_mfma_f32_32x32x16_bf16 v[64:79], a[252:255], a[188:191], v[64:79]
	s_waitcnt vmcnt(0) lgkmcnt(0)
	s_barrier
	s_mov_b32 m0, s0
	v_mfma_f32_32x32x16_bf16 a[0:15], v[172:175], v[164:167], a[0:15]
	buffer_load_dwordx4 v222, s[12:15], s1 offen lds
	s_mov_b32 m0, s35
	v_mfma_f32_32x32x16_bf16 a[16:31], v[172:175], v[192:195], a[16:31]
	buffer_load_dwordx4 v223, s[12:15], s36 offen lds
	ds_read_b128 a[192:195], v217 offset:0
	s_mov_b32 m0, s37
	v_mfma_f32_32x32x16_bf16 a[32:47], v[184:187], v[164:167], a[32:47]
	v_add_f32_e32 v225, v225, v156
	v_add_f32_e32 v156, v159, v158
	buffer_load_dwordx4 v222, s[12:15], s38 offen lds
	ds_read_b128 a[196:199], v199 offset:0
	s_mov_b32 m0, s39
	v_mfma_f32_32x32x16_bf16 a[48:63], v[184:187], v[192:195], a[48:63]
	buffer_load_dwordx4 v223, s[12:15], s40 offen lds
	ds_read_b128 a[200:203], v198 offset:0
	s_mov_b32 m0, s41
	v_mfma_f32_32x32x16_bf16 a[64:79], v[180:183], v[164:167], a[64:79]
	v_add_f32_e32 v226, v226, v156
	buffer_load_dwordx4 v196, s[4:7], s42 offen lds
	ds_read_b128 a[204:207], v197 offset:0
	s_mov_b32 m0, s43
	v_mfma_f32_32x32x16_bf16 a[80:95], v[180:183], v[192:195], a[80:95]
	buffer_load_dwordx4 v196, s[4:7], s44 offen lds
	ds_read_b128 a[208:211], v217 offset:128
	s_mov_b32 m0, s45
	v_mfma_f32_32x32x16_bf16 a[96:111], v[188:191], v[164:167], a[96:111]
	buffer_load_dwordx4 v196, s[4:7], s46 offen lds
	ds_read_b128 a[212:215], v199 offset:128
	s_mov_b32 m0, s47
	v_mfma_f32_32x32x16_bf16 a[112:127], v[188:191], v[192:195], a[112:127]
	buffer_load_dwordx4 v196, s[4:7], s48 offen lds
	ds_read_b128 a[216:219], v198 offset:128
	s_nop 0
	v_mfma_f32_32x32x16_bf16 a[0:15], v[176:179], v[128:131], a[0:15]
	ds_read_b128 a[220:223], v197 offset:128
	s_cmp_gt_u32 s27, 12
	s_cbranch_scc1 .Lka_done
	s_cmp_gt_u32 s27, 4
	s_cbranch_scc1 .Lka_single
	v_cvt_pk_bf16_f32 v248, v248, v249
	v_cvt_pk_bf16_f32 v249, v250, v251
	v_cvt_pk_bf16_f32 v250, v252, v253
	v_cvt_pk_bf16_f32 v251, v254, v255
	v_lshrrev_b32_e32 v252, 1, v208
	buffer_store_dwordx4 v[248:251], v252, s[12:15], s56 offen sc1
	v_mbcnt_lo_u32_b32 v253, -1, 0
	v_mbcnt_hi_u32_b32 v253, -1, v253
	v_lshlrev_b32_e32 v253, 4, v253
	v_add_u32_e32 v253, s84, v253
	ds_read_b128 v[248:251], v253
	ds_read_b128 v[252:255], v253 offset:1024
	s_cmp_eq_u32 s27, 2
	s_cbranch_scc0 .Lka_nopub
	s_cmp_eq_u32 s50, 0
	s_cbranch_scc0 .Lf1_pub_done
	v_mov_b32_e32 v210, s70
	s_mov_b64 exec, 1
	global_store_dword v209, v210, s[72:73] offset:3072 sc1
	s_mov_b64 exec, -1

.LBB0_19:
	s_waitcnt lgkmcnt(0)
	v_mfma_f32_32x32x16_bf16 v[112:127], a[192:195], a[128:131], v[0:15]
	v_exp_f32_e32 v80, v80
	v_exp_f32_e32 v81, v81
	ds_read_b64_tr_b16 v[180:181], v212 offset:0
	v_mfma_f32_32x32x16_bf16 v[96:111], a[192:195], a[160:163], v[16:31]
	v_cvt_pk_bf16_f32 v168, v128, v129
	v_exp_f32_e32 v82, v82
	v_exp_f32_e32 v83, v83
	v_mfma_f32_32x32x16_bf16 v[48:63], a[224:227], a[128:131], v[0:15]
	ds_read_b64_tr_b16 v[182:183], v212 offset:0x800
	v_cvt_pk_bf16_f32 v169, v130, v131
	ds_read_b64_tr_b16 v[184:185], v212 offset:0x200
	v_exp_f32_e32 v239, v84
	v_mfma_f32_32x32x16_bf16 v[32:47], a[224:227], a[160:163], v[16:31]
	v_exp_f32_e32 v240, v85
	v_cvt_pk_bf16_f32 v170, v132, v133
	ds_read_b64_tr_b16 v[186:187], v212 offset:0xa00
	ds_read_b64_tr_b16 v[176:177], v212 offset:0x400
	v_mfma_f32_32x32x16_bf16 v[112:127], a[196:199], a[132:135], v[112:127]
	v_exp_f32_e32 v241, v86
	v_exp_f32_e32 v242, v87
	v_cvt_pk_bf16_f32 v171, v134, v135
	v_mfma_f32_32x32x16_bf16 v[96:111], a[196:199], a[164:167], v[96:111]
	v_exp_f32_e32 v227, v88
	v_exp_f32_e32 v228, v89
	ds_read_b64_tr_b16 v[178:179], v212 offset:0xc00
	v_mfma_f32_32x32x16_bf16 v[48:63], a[228:231], a[132:135], v[48:63]
	v_cvt_pk_bf16_f32 v128, v136, v137
	v_exp_f32_e32 v229, v90
	v_exp_f32_e32 v230, v91
	v_mfma_f32_32x32x16_bf16 v[32:47], a[228:231], a[164:167], v[32:47]
	ds_read_b64_tr_b16 v[188:189], v212 offset:0x600
	v_cvt_pk_bf16_f32 v129, v138, v139
	v_exp_f32_e32 v231, v92
	v_exp_f32_e32 v232, v93
	v_mfma_f32_32x32x16_bf16 v[112:127], a[200:203], a[136:139], v[112:127]
	ds_read_b64_tr_b16 v[190:191], v212 offset:0xe00
	v_cvt_pk_bf16_f32 v130, v140, v141
	ds_read_b64_tr_b16 v[172:173], v212 offset:0x1000
	v_exp_f32_e32 v233, v94
	v_mfma_f32_32x32x16_bf16 v[96:111], a[200:203], a[168:171], v[96:111]
	v_exp_f32_e32 v234, v95
	ds_read_b64_tr_b16 v[174:175], v212 offset:0x1800
	v_cvt_pk_bf16_f32 v131, v142, v143
	v_exp_f32_e32 v141, v64
	v_mfma_f32_32x32x16_bf16 v[48:63], a[232:235], a[136:139], v[48:63]
	v_exp_f32_e32 v142, v65
	ds_read_b64_tr_b16 v[164:165], v212 offset:0x1200
	v_cvt_pk_bf16_f32 v192, v144, v145
	v_exp_f32_e32 v143, v66
	v_mfma_f32_32x32x16_bf16 v[32:47], a[232:235], a[168:171], v[32:47]
	ds_read_b64_tr_b16 v[166:167], v212 offset:0x1a00
	v_exp_f32_e32 v243, v67
	v_cvt_pk_bf16_f32 v193, v146, v147
	ds_read_b64_tr_b16 v[160:161], v212 offset:0x1400
	v_mfma_f32_32x32x16_bf16 v[112:127], a[204:207], a[140:143], v[112:127]
	v_exp_f32_e32 v244, v68
	v_exp_f32_e32 v245, v69
	v_cvt_pk_bf16_f32 v194, v148, v149
	v_mfma_f32_32x32x16_bf16 v[96:111], a[204:207], a[172:175], v[96:111]
	ds_read_b64_tr_b16 v[162:163], v212 offset:0x1c00
	ds_read_b64_tr_b16 v[136:137], v212 offset:0x1600
	v_exp_f32_e32 v246, v70
	v_exp_f32_e32 v247, v71
	v_mfma_f32_32x32x16_bf16 v[48:63], a[236:239], a[140:143], v[48:63]
	v_cvt_pk_bf16_f32 v195, v150, v151
	v_exp_f32_e32 v148, v72
	v_exp_f32_e32 v149, v73
	v_mfma_f32_32x32x16_bf16 v[32:47], a[236:239], a[172:175], v[32:47]
	ds_read_b64_tr_b16 v[138:139], v212 offset:0x1e00
	v_cvt_pk_bf16_f32 v144, v152, v153
	v_exp_f32_e32 v150, v74
	v_exp_f32_e32 v151, v75
	v_mfma_f32_32x32x16_bf16 v[112:127], a[208:211], a[144:147], v[112:127]
	ds_read_b64_tr_b16 v[132:133], v212 offset:0x2000
	v_cvt_pk_bf16_f32 v145, v154, v155
	v_exp_f32_e32 v152, v76
	v_exp_f32_e32 v153, v77
	v_mfma_f32_32x32x16_bf16 v[96:111], a[208:211], a[176:179], v[96:111]
	ds_read_b64_tr_b16 v[134:135], v212 offset:0x2800
	v_cvt_pk_bf16_f32 v146, v156, v157
	ds_read_b64_tr_b16 v[92:93], v212 offset:0x2200
	v_exp_f32_e32 v154, v78
	v_mfma_f32_32x32x16_bf16 v[48:63], a[240:243], a[144:147], v[48:63]
	v_exp_f32_e32 v155, v79
	ds_read_b64_tr_b16 v[94:95], v212 offset:0x2a00
	v_cvt_pk_bf16_f32 v147, v158, v159
	s_mov_b32 s0, s3
	ds_read_b64_tr_b16 v[88:89], v212 offset:0x2400
	v_mfma_f32_32x32x16_bf16 v[32:47], a[240:243], a[176:179], v[32:47]
	v_cvt_pk_bf16_f32 v84, v80, v81
	v_add_f32_e32 v64, v236, v80
	v_add_f32_e32 v65, v235, v81
	s_add_i32 s58, s57, s60
	s_and_b32 s58, s58, 0x7ffff
	s_mov_b32 s1, s58
	ds_read_b64_tr_b16 v[90:91], v212 offset:0x2c00
	v_mfma_f32_32x32x16_bf16 v[112:127], a[212:215], a[148:151], v[112:127]
	v_cvt_pk_bf16_f32 v85, v82, v83
	v_add_f32_e32 v64, v64, v82
	v_add_f32_e32 v65, v65, v83
	s_mov_b32 s35, s10
	ds_read_b64_tr_b16 v[80:81], v212 offset:0x2600
	v_cvt_pk_bf16_f32 v86, v239, v240
	v_mfma_f32_32x32x16_bf16 v[96:111], a[212:215], a[180:183], v[96:111]
	v_add_f32_e32 v64, v64, v239
	v_add_f32_e32 v65, v65, v240
	s_add_i32 s36, s58, 0x400
	ds_read_b64_tr_b16 v[82:83], v212 offset:0x2e00
	ds_read_b64_tr_b16 v[76:77], v212 offset:0x3000
	v_cvt_pk_bf16_f32 v87, v241, v242
	v_mfma_f32_32x32x16_bf16 v[48:63], a[244:247], a[148:151], v[48:63]
	v_add_f32_e32 v64, v64, v241
	v_add_f32_e32 v65, v65, v242
	s_mov_b32 s37, s11
	ds_read_b64_tr_b16 v[78:79], v212 offset:0x3800
	v_add_f32_e32 v64, v64, v227
	v_add_f32_e32 v65, v65, v228
	v_mfma_f32_32x32x16_bf16 v[32:47], a[244:247], a[180:183], v[32:47]
	s_add_i32 s38, s58, 0x800
	ds_read_b64_tr_b16 v[72:73], v212 offset:0x3200
	v_add_f32_e32 v64, v64, v229
	v_add_f32_e32 v65, v65, v230
	s_mov_b32 s39, s16
	ds_read_b64_tr_b16 v[74:75], v212 offset:0x3a00
	v_mfma_f32_32x32x16_bf16 v[112:127], a[216:219], a[152:155], v[112:127]
	v_add_f32_e32 v64, v64, v231
	v_add_f32_e32 v65, v65, v232
	s_add_i32 s40, s58, 0xc00
	ds_read_b64_tr_b16 v[68:69], v212 offset:0x3400
	ds_read_b64_tr_b16 v[70:71], v212 offset:0x3c00
	v_add_f32_e32 v156, v64, v233
	v_mfma_f32_32x32x16_bf16 v[96:111], a[216:219], a[184:187], v[96:111]
	v_add_f32_e32 v157, v65, v234
	s_mov_b32 s41, s2
	ds_read_b64_tr_b16 v[64:65], v212 offset:0x3600
	v_cvt_pk_bf16_f32 v140, v141, v142
	v_add_f32_e32 v158, v237, v141
	v_add_f32_e32 v142, v238, v142
	v_mfma_f32_32x32x16_bf16 v[48:63], a[248:251], a[152:155], v[48:63]
	ds_read_b64_tr_b16 v[66:67], v212 offset:0x3e00
	v_cvt_pk_bf16_f32 v141, v143, v243
	v_add_f32_e32 v143, v158, v143
	v_add_f32_e32 v158, v142, v243
	s_mov_b32 s42, s17
	v_cvt_pk_bf16_f32 v142, v244, v245
	v_mfma_f32_32x32x16_bf16 v[32:47], a[248:251], a[184:187], v[32:47]
	v_add_f32_e32 v159, v143, v244
	v_add_f32_e32 v158, v158, v245
	s_add_i32 s43, s57, 0x80
	v_cvt_pk_bf16_f32 v143, v246, v247
	v_add_f32_e32 v159, v159, v246
	v_add_f32_e32 v158, v158, v247
	v_mfma_f32_32x32x16_bf16 v[112:127], a[220:223], a[156:159], v[112:127]
	s_mov_b32 s44, s18
	v_add_f32_e32 v159, v159, v148
	v_add_f32_e32 v158, v158, v149
	v_add_f32_e32 v159, v159, v150
	v_add_f32_e32 v158, v158, v151
	s_mov_b32 s45, s19
	v_mfma_f32_32x32x16_bf16 v[96:111], a[220:223], a[188:191], v[96:111]
	v_add_f32_e32 v159, v159, v152
	v_add_f32_e32 v158, v158, v153
	s_add_i32 s46, s57, 0x880
	v_add_f32_e32 v159, v159, v154
	v_add_f32_e32 v158, v158, v155
	v_add_f32_e32 v156, v156, v157
	v_mfma_f32_32x32x16_bf16 v[48:63], a[252:255], a[156:159], v[48:63]
	v_mfma_f32_32x32x16_bf16 v[32:47], a[252:255], a[188:191], v[32:47]
	s_waitcnt vmcnt(0) lgkmcnt(0)
	s_barrier
	s_mov_b32 m0, s0
	v_mfma_f32_32x32x16_bf16 a[0:15], v[180:183], v[168:171], a[0:15]
	buffer_load_dwordx4 v222, s[12:15], s1 offen lds
	s_mov_b32 m0, s35
	v_mfma_f32_32x32x16_bf16 a[16:31], v[180:183], v[192:195], a[16:31]
	buffer_load_dwordx4 v223, s[12:15], s36 offen lds
	ds_read_b128 a[192:195], v218 offset:0
	s_mov_b32 m0, s37
	v_mfma_f32_32x32x16_bf16 a[32:47], v[184:187], v[168:171], a[32:47]
	v_add_f32_e32 v225, v225, v156
	v_add_f32_e32 v156, v159, v158
	buffer_load_dwordx4 v222, s[12:15], s38 offen lds
	ds_read_b128 a[196:199], v219 offset:0
	s_mov_b32 m0, s39
	v_mfma_f32_32x32x16_bf16 a[48:63], v[184:187], v[192:195], a[48:63]
	buffer_load_dwordx4 v223, s[12:15], s40 offen lds
	ds_read_b128 a[200:203], v220 offset:0
	s_mov_b32 m0, s41
	v_mfma_f32_32x32x16_bf16 a[64:79], v[176:179], v[168:171], a[64:79]
	v_add_f32_e32 v226, v226, v156
	buffer_load_dwordx4 v196, s[4:7], s33 offen lds
	ds_read_b128 a[204:207], v221 offset:0
	s_mov_b32 m0, s42
	v_mfma_f32_32x32x16_bf16 a[80:95], v[176:179], v[192:195], a[80:95]
	buffer_load_dwordx4 v196, s[4:7], s43 offen lds
	ds_read_b128 a[208:211], v218 offset:128
	s_mov_b32 m0, s44
	v_mfma_f32_32x32x16_bf16 a[96:111], v[188:191], v[168:171], a[96:111]
	buffer_load_dwordx4 v196, s[4:7], s34 offen lds
	ds_read_b128 a[212:215], v219 offset:128
	s_mov_b32 m0, s45
	v_mfma_f32_32x32x16_bf16 a[112:127], v[188:191], v[192:195], a[112:127]
	buffer_load_dwordx4 v196, s[4:7], s46 offen lds
	ds_read_b128 a[216:219], v220 offset:128
	s_nop 0
	v_mfma_f32_32x32x16_bf16 a[0:15], v[172:175], v[128:131], a[0:15]
	ds_read_b128 a[220:223], v221 offset:128
	s_cmp_gt_u32 s27, 12
	s_cbranch_scc1 .Lkc_done
	s_cmp_gt_u32 s27, 4
	s_cbranch_scc1 .Lkc_single
	v_cvt_pk_bf16_f32 v248, v248, v249
	v_cvt_pk_bf16_f32 v249, v250, v251
	v_cvt_pk_bf16_f32 v250, v252, v253
	v_cvt_pk_bf16_f32 v251, v254, v255
	v_lshrrev_b32_e32 v252, 1, v208
	buffer_store_dwordx4 v[248:251], v252, s[12:15], s56 offen sc1
	v_mbcnt_lo_u32_b32 v253, -1, 0
	v_mbcnt_hi_u32_b32 v253, -1, v253
	v_lshlrev_b32_e32 v253, 4, v253
	v_add_u32_e32 v253, s84, v253
	ds_read_b128 v[248:251], v253
	ds_read_b128 v[252:255], v253 offset:1024
	s_branch .Lkc_done
